# v30
# speedup vs baseline: 1.0082x; 1.0006x over previous
.LBB2_35:
	s_lshl_b32 s28, s27, 2
	v_add_u32_e32 v79, s28, v3
	v_lshl_add_u32 v79, v79, 2, v2
	ds_read_b32 v80, v79 offset:15360
	ds_read_b32 v81, v79 offset:15364
	ds_read_b32 v82, v79 offset:15368
	ds_read_b32 v79, v79 offset:15372
	v_cmp_lt_i32_e32 vcc, s28, v5
	s_or_b32 s29, s28, 1
	s_or_b32 s30, s28, 2
	s_waitcnt lgkmcnt(0)
	v_cndmask_b32_e32 v87, v9, v80, vcc
	v_cmp_lt_i32_e32 vcc, s29, v5
	s_or_b32 s31, s28, 3
	s_nop 0
	v_cndmask_b32_e32 v88, v9, v81, vcc
	v_cmp_lt_i32_e32 vcc, s30, v5
	v_lshl_or_b32 v83, v87, 7, v66
	v_lshlrev_b32_e32 v87, 2, v87
	v_cndmask_b32_e32 v89, v9, v82, vcc
	v_cmp_lt_i32_e32 vcc, s31, v5
	v_lshl_or_b32 v84, v88, 7, v66
	v_lshl_or_b32 v85, v89, 7, v66
	v_cndmask_b32_e32 v90, v9, v79, vcc
	v_lshl_or_b32 v86, v90, 7, v66
	v_lshlrev_b32_e32 v88, 2, v88
	v_lshlrev_b32_e32 v89, 2, v89
	v_lshlrev_b32_e32 v90, 2, v90
	s_waitcnt vmcnt(10)
	v_cvt_pk_f16_f32 v10, v61, v62
	v_perm_b32 v11, v40, v38, s23
	v_dot2c_f32_f16_e32 v60, v11, v10
	v_perm_b32 v11, v40, v38, s24
	v_dot2c_f32_f16_e32 v42, v11, v10
	v_perm_b32 v11, v40, v38, s25
	v_dot2c_f32_f16_e32 v43, v11, v10
	v_perm_b32 v11, v40, v38, s26
	v_dot2c_f32_f16_e32 v36, v11, v10
	v_perm_b32 v11, v41, v39, s23
	v_dot2c_f32_f16_e32 v37, v11, v10
	v_perm_b32 v11, v41, v39, s24
	v_dot2c_f32_f16_e32 v30, v11, v10
	v_perm_b32 v11, v41, v39, s25
	v_dot2c_f32_f16_e32 v31, v11, v10
	v_perm_b32 v11, v41, v39, s26
	v_dot2c_f32_f16_e32 v53, v11, v10
	v_dot2c_f32_f16_e32 v45, 0x3c003c00, v10
	s_waitcnt vmcnt(8)
	v_cvt_pk_f16_f32 v10, v58, v59
	v_perm_b32 v11, v34, v32, s23
	v_dot2c_f32_f16_e32 v60, v11, v10
	v_perm_b32 v11, v34, v32, s24
	v_dot2c_f32_f16_e32 v42, v11, v10
	v_perm_b32 v11, v34, v32, s25
	v_dot2c_f32_f16_e32 v43, v11, v10
	v_perm_b32 v11, v34, v32, s26
	v_dot2c_f32_f16_e32 v36, v11, v10
	v_perm_b32 v11, v35, v33, s23
	v_dot2c_f32_f16_e32 v37, v11, v10
	v_perm_b32 v11, v35, v33, s24
	v_dot2c_f32_f16_e32 v30, v11, v10
	v_perm_b32 v11, v35, v33, s25
	v_dot2c_f32_f16_e32 v31, v11, v10
	v_perm_b32 v11, v35, v33, s26
	s_add_i32 s5, s5, 1
	v_dot2c_f32_f16_e32 v53, v11, v10
	s_cmp_lg_u32 s5, s4
	v_dot2c_f32_f16_e32 v45, 0x3c003c00, v10
	s_cbranch_scc0 .Lfl2_a
.LBB2_43:
	s_add_i32 s27, s27, 1
	global_load_dwordx2 v[38:39], v83, s[10:11]
	global_load_dwordx2 v[40:41], v84, s[10:11]
	global_load_dwordx2 v[32:33], v85, s[10:11]
	global_load_dwordx2 v[34:35], v86, s[10:11]
	global_load_dword v61, v87, s[12:13]
	global_load_dword v62, v88, s[12:13]
	global_load_dword v58, v89, s[12:13]
	global_load_dword v59, v90, s[12:13]
	s_cmp_lg_u32 s27, s21
	s_cbranch_scc0 .Lcu2_a
.LBB2_49:
	s_lshl_b32 s28, s27, 2
	v_add_u32_e32 v79, s28, v3
	v_lshl_add_u32 v79, v79, 2, v2
	ds_read_b32 v80, v79 offset:15360
	ds_read_b32 v81, v79 offset:15364
	ds_read_b32 v82, v79 offset:15368
	ds_read_b32 v79, v79 offset:15372
	v_cmp_lt_i32_e32 vcc, s28, v5
	s_or_b32 s29, s28, 1
	s_or_b32 s30, s28, 2
	s_waitcnt lgkmcnt(0)
	v_cndmask_b32_e32 v87, v9, v80, vcc
	v_cmp_lt_i32_e32 vcc, s29, v5
	s_or_b32 s31, s28, 3
	s_nop 0
	v_cndmask_b32_e32 v88, v9, v81, vcc
	v_cmp_lt_i32_e32 vcc, s30, v5
	v_lshl_or_b32 v83, v87, 7, v66
	v_lshlrev_b32_e32 v87, 2, v87
	v_cndmask_b32_e32 v89, v9, v82, vcc
	v_cmp_lt_i32_e32 vcc, s31, v5
	v_lshl_or_b32 v84, v88, 7, v66
	v_lshl_or_b32 v85, v89, 7, v66
	v_cndmask_b32_e32 v90, v9, v79, vcc
	v_lshl_or_b32 v86, v90, 7, v66
	v_lshlrev_b32_e32 v88, 2, v88
	v_lshlrev_b32_e32 v89, 2, v89
	v_lshlrev_b32_e32 v90, 2, v90
	s_waitcnt vmcnt(10)
	v_cvt_pk_f16_f32 v10, v56, v57
	v_perm_b32 v11, v28, v26, s23
	v_dot2c_f32_f16_e32 v60, v11, v10
	v_perm_b32 v11, v28, v26, s24
	v_dot2c_f32_f16_e32 v42, v11, v10
	v_perm_b32 v11, v28, v26, s25
	v_dot2c_f32_f16_e32 v43, v11, v10
	v_perm_b32 v11, v28, v26, s26
	v_dot2c_f32_f16_e32 v36, v11, v10
	v_perm_b32 v11, v29, v27, s23
	v_dot2c_f32_f16_e32 v37, v11, v10
	v_perm_b32 v11, v29, v27, s24
	v_dot2c_f32_f16_e32 v30, v11, v10
	v_perm_b32 v11, v29, v27, s25
	v_dot2c_f32_f16_e32 v31, v11, v10
	v_perm_b32 v11, v29, v27, s26
	v_dot2c_f32_f16_e32 v53, v11, v10
	v_dot2c_f32_f16_e32 v45, 0x3c003c00, v10
	s_waitcnt vmcnt(8)
	v_cvt_pk_f16_f32 v10, v54, v55
	v_perm_b32 v11, v24, v22, s23
	v_dot2c_f32_f16_e32 v60, v11, v10
	v_perm_b32 v11, v24, v22, s24
	v_dot2c_f32_f16_e32 v42, v11, v10
	v_perm_b32 v11, v24, v22, s25
	v_dot2c_f32_f16_e32 v43, v11, v10
	v_perm_b32 v11, v24, v22, s26
	v_dot2c_f32_f16_e32 v36, v11, v10
	v_perm_b32 v11, v25, v23, s23
	v_dot2c_f32_f16_e32 v37, v11, v10
	v_perm_b32 v11, v25, v23, s24
	v_dot2c_f32_f16_e32 v30, v11, v10
	v_perm_b32 v11, v25, v23, s25
	v_dot2c_f32_f16_e32 v31, v11, v10
	v_perm_b32 v11, v25, v23, s26
	s_add_i32 s5, s5, 1
	v_dot2c_f32_f16_e32 v53, v11, v10
	s_cmp_lg_u32 s5, s4
	v_dot2c_f32_f16_e32 v45, 0x3c003c00, v10
	s_cbranch_scc0 .Lfl2_b
.LBB2_57:
	s_add_i32 s27, s27, 1
	global_load_dwordx2 v[26:27], v83, s[10:11]
	global_load_dwordx2 v[28:29], v84, s[10:11]
	global_load_dwordx2 v[22:23], v85, s[10:11]
	global_load_dwordx2 v[24:25], v86, s[10:11]
	global_load_dword v56, v87, s[12:13]
	global_load_dword v57, v88, s[12:13]
	global_load_dword v54, v89, s[12:13]
	global_load_dword v55, v90, s[12:13]
	s_cmp_lg_u32 s27, s21
	s_cbranch_scc0 .Lcu2_b
	s_add_i32 s22, s22, -1
	s_cmp_lg_u32 s22, 0
	s_cbranch_scc1 .LBB2_35
	s_branch .LBB2_84
.Lfl2_a:
	v_cmp_gt_i32_e32 vcc, 15, v18
	s_and_saveexec_b64 s[4:5], vcc
	s_cbranch_execz .LBB2_38
	v_max_i32_e32 v10, 1, v44
	v_cvt_f32_u32_e32 v10, v10
	v_rcp_iflag_f32_e32 v44, v10
	s_nop 0
	v_pk_mul_f32 v[10:11], v[44:45], s[2:3]
	s_nop 0
	v_mul_f32_e32 v14, 0x4b800000, v10
	v_pk_mul_f32 v[16:17], v[10:11], v[10:11] op_sel:[0,1] op_sel_hi:[1,0]
	s_nop 0
	v_fma_mixlo_f16 v15, v60, v14, v16
	v_pk_fma_f32 v[10:11], v[42:43], v[14:15], v[16:17] op_sel_hi:[1,0,0]
	v_pk_fma_f32 v[12:13], v[36:37], v[14:15], v[16:17] op_sel_hi:[1,0,0]
	v_pk_fma_f32 v[30:31], v[30:31], v[14:15], v[16:17] op_sel_hi:[1,0,0]
	v_cvt_pk_f16_f32 v11, v10, v11
	v_cvt_pk_f16_f32 v12, v12, v13
	v_cvt_pk_f16_f32 v13, v30, v31
	v_pack_b32_f16 v10, v15, v11
	v_alignbit_b32 v11, v12, v11, 16
	v_alignbit_b32 v12, v13, v12, 16
	v_lshrrev_b32_e32 v13, 16, v13
	v_fma_mixhi_f16 v13, v53, v14, v16
	v_add_u32_e32 v14, v18, v77
	v_xor_b32_e32 v15, v14, v0
	v_lshlrev_b32_e32 v15, 4, v15
	v_and_b32_e32 v15, 0xf0, v15
	v_lshl_or_b32 v14, v14, 8, v15
	ds_write_b128 v14, v[10:13]

.LBB2_42:
	s_mov_b32 s5, 0
	v_mov_b32_e32 v53, 0
	v_mov_b32_e32 v31, 0
	v_mov_b32_e32 v30, 0
	v_mov_b32_e32 v37, 0
	v_mov_b32_e32 v36, 0
	v_mov_b32_e32 v43, 0
	v_mov_b32_e32 v42, 0
	v_mov_b32_e32 v60, 0
	v_mov_b32_e32 v45, 0
	s_branch .LBB2_43
.Lcu2_a:
	s_cmp_eq_u32 s20, 0
	s_cbranch_scc1 .LBB2_47
	s_add_i32 s27, s20, 1
	s_mov_b32 s20, 2
	s_cmp_eq_u32 s27, 2
	v_mov_b32_e32 v3, v7
	v_mov_b32_e32 v5, v51
	s_mov_b32 s21, s16
	s_cbranch_scc1 .LBB2_48
	s_cmp_eq_u32 s27, 3
	s_cselect_b64 vcc, -1, 0
	s_and_b64 s[20:21], vcc, exec
	v_cndmask_b32_e32 v5, 0, v52, vcc
	s_cselect_b32 s21, s6, 0x7fffffff
	s_mov_b32 s20, s27
	v_mov_b32_e32 v3, v8
	s_branch .LBB2_48

.LBB2_48:
	s_mov_b32 s27, 0
	s_branch .LBB2_49
.Lfl2_b:
	v_cmp_gt_i32_e32 vcc, 15, v18
	s_and_saveexec_b64 s[4:5], vcc
	s_cbranch_execz .LBB2_52
	v_max_i32_e32 v10, 1, v44
	v_cvt_f32_u32_e32 v10, v10
	v_rcp_iflag_f32_e32 v44, v10
	s_nop 0
	v_pk_mul_f32 v[10:11], v[44:45], s[2:3]
	s_nop 0
	v_mul_f32_e32 v14, 0x4b800000, v10
	v_pk_mul_f32 v[16:17], v[10:11], v[10:11] op_sel:[0,1] op_sel_hi:[1,0]
	s_nop 0
	v_fma_mixlo_f16 v15, v60, v14, v16
	v_pk_fma_f32 v[10:11], v[42:43], v[14:15], v[16:17] op_sel_hi:[1,0,0]
	v_pk_fma_f32 v[12:13], v[36:37], v[14:15], v[16:17] op_sel_hi:[1,0,0]
	v_pk_fma_f32 v[22:23], v[30:31], v[14:15], v[16:17] op_sel_hi:[1,0,0]
	v_cvt_pk_f16_f32 v11, v10, v11
	v_cvt_pk_f16_f32 v12, v12, v13
	v_cvt_pk_f16_f32 v13, v22, v23
	v_pack_b32_f16 v10, v15, v11
	v_alignbit_b32 v11, v12, v11, 16
	v_alignbit_b32 v12, v13, v12, 16
	v_lshrrev_b32_e32 v13, 16, v13
	v_fma_mixhi_f16 v13, v53, v14, v16
	v_add_u32_e32 v14, v18, v77
	v_xor_b32_e32 v15, v14, v0
	v_lshlrev_b32_e32 v15, 4, v15
	v_and_b32_e32 v15, 0xf0, v15
	v_lshl_or_b32 v14, v14, 8, v15
	ds_write_b128 v14, v[10:13]

.LBB2_107:
	s_or_b64 exec, exec, s[2:3]
	s_load_dwordx4 s[4:7], s[0:1], 0x38
	s_cmpk_lt_i32 s19, 0x181
	s_cbranch_scc0 .LBB2_62
	s_branch .LBB2_63
	s_nop 0
	s_nop 0
	s_nop 0
	s_endpgm

.LBB3_33:
	s_lshl_b32 s26, s25, 2
	v_add_u32_e32 v82, s26, v3
	v_lshl_add_u32 v82, v82, 2, v2
	ds_read_b32 v83, v82 offset:15360
	ds_read_b32 v84, v82 offset:15364
	ds_read_b32 v85, v82 offset:15368
	ds_read_b32 v82, v82 offset:15372
	v_cmp_lt_i32_e32 vcc, s26, v5
	s_or_b32 s28, s26, 1
	s_or_b32 s29, s26, 2
	s_waitcnt lgkmcnt(0)
	v_cndmask_b32_e32 v87, v8, v83, vcc
	v_cmp_lt_i32_e32 vcc, s28, v5
	s_or_b32 s30, s26, 3
	s_nop 0
	v_cndmask_b32_e32 v88, v8, v84, vcc
	v_cmp_lt_i32_e32 vcc, s29, v5
	v_lshl_or_b32 v79, v87, 7, v78
	v_lshlrev_b32_e32 v87, 2, v87
	v_cndmask_b32_e32 v89, v8, v85, vcc
	v_cmp_lt_i32_e32 vcc, s30, v5
	v_lshl_or_b32 v80, v88, 7, v78
	v_lshl_or_b32 v81, v89, 7, v78
	v_cndmask_b32_e32 v90, v8, v82, vcc
	v_lshl_or_b32 v86, v90, 7, v78
	v_lshlrev_b32_e32 v88, 2, v88
	v_lshlrev_b32_e32 v89, 2, v89
	v_lshlrev_b32_e32 v90, 2, v90
	s_waitcnt vmcnt(10)
	v_cvt_pk_f16_f32 v9, v57, v58
	v_perm_b32 v10, v40, v38, s21
	v_dot2c_f32_f16_e32 v56, v10, v9
	v_perm_b32 v10, v40, v38, s22
	v_dot2c_f32_f16_e32 v42, v10, v9
	v_perm_b32 v10, v40, v38, s23
	v_dot2c_f32_f16_e32 v43, v10, v9
	v_perm_b32 v10, v40, v38, s24
	v_dot2c_f32_f16_e32 v36, v10, v9
	v_perm_b32 v10, v41, v39, s21
	v_dot2c_f32_f16_e32 v37, v10, v9
	v_perm_b32 v10, v41, v39, s22
	v_dot2c_f32_f16_e32 v30, v10, v9
	v_perm_b32 v10, v41, v39, s23
	v_dot2c_f32_f16_e32 v31, v10, v9
	v_perm_b32 v10, v41, v39, s24
	v_dot2c_f32_f16_e32 v49, v10, v9
	s_waitcnt vmcnt(8)
	v_cvt_pk_f16_f32 v9, v54, v55
	v_perm_b32 v10, v34, v32, s21
	v_dot2c_f32_f16_e32 v56, v10, v9
	v_perm_b32 v10, v34, v32, s22
	v_dot2c_f32_f16_e32 v42, v10, v9
	v_perm_b32 v10, v34, v32, s23
	v_dot2c_f32_f16_e32 v43, v10, v9
	v_perm_b32 v10, v34, v32, s24
	v_dot2c_f32_f16_e32 v36, v10, v9
	v_perm_b32 v10, v35, v33, s21
	v_dot2c_f32_f16_e32 v37, v10, v9
	v_perm_b32 v10, v35, v33, s22
	v_dot2c_f32_f16_e32 v30, v10, v9
	v_perm_b32 v10, v35, v33, s23
	v_dot2c_f32_f16_e32 v31, v10, v9
	v_perm_b32 v10, v35, v33, s24
	s_add_i32 s5, s5, 1
	v_dot2c_f32_f16_e32 v49, v10, v9
	s_cmp_lg_u32 s5, s4
	s_cbranch_scc0 .Lfl3_a
.LBB3_41:
	s_add_i32 s25, s25, 1
	global_load_dwordx2 v[38:39], v79, s[10:11]
	global_load_dwordx2 v[40:41], v80, s[10:11]
	global_load_dwordx2 v[32:33], v81, s[10:11]
	global_load_dwordx2 v[34:35], v86, s[10:11]
	global_load_dword v57, v87, s[12:13]
	global_load_dword v58, v88, s[12:13]
	global_load_dword v54, v89, s[12:13]
	global_load_dword v55, v90, s[12:13]
	s_cmp_lg_u32 s25, s19
	s_cbranch_scc0 .Lcu3_a
.LBB3_47:
	s_lshl_b32 s26, s25, 2
	v_add_u32_e32 v82, s26, v3
	v_lshl_add_u32 v82, v82, 2, v2
	ds_read_b32 v83, v82 offset:15360
	ds_read_b32 v84, v82 offset:15364
	ds_read_b32 v85, v82 offset:15368
	ds_read_b32 v82, v82 offset:15372
	v_cmp_lt_i32_e32 vcc, s26, v5
	s_or_b32 s28, s26, 1
	s_or_b32 s29, s26, 2
	s_waitcnt lgkmcnt(0)
	v_cndmask_b32_e32 v87, v8, v83, vcc
	v_cmp_lt_i32_e32 vcc, s28, v5
	s_or_b32 s30, s26, 3
	s_nop 0
	v_cndmask_b32_e32 v88, v8, v84, vcc
	v_cmp_lt_i32_e32 vcc, s29, v5
	v_lshl_or_b32 v79, v87, 7, v78
	v_lshlrev_b32_e32 v87, 2, v87
	v_cndmask_b32_e32 v89, v8, v85, vcc
	v_cmp_lt_i32_e32 vcc, s30, v5
	v_lshl_or_b32 v80, v88, 7, v78
	v_lshl_or_b32 v81, v89, 7, v78
	v_cndmask_b32_e32 v90, v8, v82, vcc
	v_lshl_or_b32 v86, v90, 7, v78
	v_lshlrev_b32_e32 v88, 2, v88
	v_lshlrev_b32_e32 v89, 2, v89
	v_lshlrev_b32_e32 v90, 2, v90
	s_waitcnt vmcnt(10)
	v_cvt_pk_f16_f32 v9, v52, v53
	v_perm_b32 v10, v28, v26, s21
	v_dot2c_f32_f16_e32 v56, v10, v9
	v_perm_b32 v10, v28, v26, s22
	v_dot2c_f32_f16_e32 v42, v10, v9
	v_perm_b32 v10, v28, v26, s23
	v_dot2c_f32_f16_e32 v43, v10, v9
	v_perm_b32 v10, v28, v26, s24
	v_dot2c_f32_f16_e32 v36, v10, v9
	v_perm_b32 v10, v29, v27, s21
	v_dot2c_f32_f16_e32 v37, v10, v9
	v_perm_b32 v10, v29, v27, s22
	v_dot2c_f32_f16_e32 v30, v10, v9
	v_perm_b32 v10, v29, v27, s23
	v_dot2c_f32_f16_e32 v31, v10, v9
	v_perm_b32 v10, v29, v27, s24
	v_dot2c_f32_f16_e32 v49, v10, v9
	s_waitcnt vmcnt(8)
	v_cvt_pk_f16_f32 v9, v50, v51
	v_perm_b32 v10, v24, v22, s21
	v_dot2c_f32_f16_e32 v56, v10, v9
	v_perm_b32 v10, v24, v22, s22
	v_dot2c_f32_f16_e32 v42, v10, v9
	v_perm_b32 v10, v24, v22, s23
	v_dot2c_f32_f16_e32 v43, v10, v9
	v_perm_b32 v10, v24, v22, s24
	v_dot2c_f32_f16_e32 v36, v10, v9
	v_perm_b32 v10, v25, v23, s21
	v_dot2c_f32_f16_e32 v37, v10, v9
	v_perm_b32 v10, v25, v23, s22
	v_dot2c_f32_f16_e32 v30, v10, v9
	v_perm_b32 v10, v25, v23, s23
	v_dot2c_f32_f16_e32 v31, v10, v9
	v_perm_b32 v10, v25, v23, s24
	s_add_i32 s5, s5, 1
	v_dot2c_f32_f16_e32 v49, v10, v9
	s_cmp_lg_u32 s5, s4
	s_cbranch_scc0 .Lfl3_b
.LBB3_55:
	s_add_i32 s25, s25, 1
	global_load_dwordx2 v[26:27], v79, s[10:11]
	global_load_dwordx2 v[28:29], v80, s[10:11]
	global_load_dwordx2 v[22:23], v81, s[10:11]
	global_load_dwordx2 v[24:25], v86, s[10:11]
	global_load_dword v52, v87, s[12:13]
	global_load_dword v53, v88, s[12:13]
	global_load_dword v50, v89, s[12:13]
	global_load_dword v51, v90, s[12:13]
	s_cmp_lg_u32 s25, s19
	s_cbranch_scc0 .Lcu3_b
	s_add_i32 s20, s20, -1
	s_cmp_lg_u32 s20, 0
	s_cbranch_scc1 .LBB3_33
	s_branch .LBB3_86
.Lfl3_a:
	v_cmp_gt_i32_e32 vcc, 15, v18
	s_and_saveexec_b64 s[4:5], vcc
	s_cbranch_execz .LBB3_36
	v_max_i32_e32 v9, 1, v44
	v_cvt_f32_u32_e32 v9, v9
	v_rcp_iflag_f32_e32 v44, v9
	s_nop 0
	v_pk_mul_f32 v[10:11], v[44:45], s[2:3]
	s_nop 0
	v_mul_f32_e32 v14, 0x4b800000, v10
	v_pk_mul_f32 v[16:17], v[10:11], v[10:11] op_sel:[0,1] op_sel_hi:[1,0]
	s_nop 0
	v_pk_fma_f32 v[10:11], v[42:43], v[14:15], v[16:17] op_sel_hi:[1,0,0]
	v_fma_mixlo_f16 v9, v56, v14, v16
	v_pk_fma_f32 v[12:13], v[36:37], v[14:15], v[16:17] op_sel_hi:[1,0,0]
	v_pk_fma_f32 v[30:31], v[30:31], v[14:15], v[16:17] op_sel_hi:[1,0,0]
	v_cvt_pk_f16_f32 v11, v10, v11
	v_cvt_pk_f16_f32 v12, v12, v13
	v_pack_b32_f16 v10, v9, v11
	v_cvt_pk_f16_f32 v9, v30, v31
	v_alignbit_b32 v11, v12, v11, 16
	v_alignbit_b32 v12, v9, v12, 16
	v_lshrrev_b32_e32 v13, 16, v9
	v_add_u32_e32 v9, v18, v75
	v_fma_mixhi_f16 v13, v49, v14, v16
	v_xor_b32_e32 v14, v9, v0
	v_lshlrev_b32_e32 v14, 4, v14
	v_and_b32_e32 v14, 0xf0, v14
	v_lshl_or_b32 v9, v9, 8, v14
	ds_write_b128 v9, v[10:13]

.LBB3_40:
	s_mov_b32 s5, 0
	v_mov_b32_e32 v49, 0
	v_mov_b32_e32 v31, 0
	v_mov_b32_e32 v30, 0
	v_mov_b32_e32 v37, 0
	v_mov_b32_e32 v36, 0
	v_mov_b32_e32 v43, 0
	v_mov_b32_e32 v42, 0
	v_mov_b32_e32 v56, 0
	v_mov_b32_e32 v45, 0
	s_branch .LBB3_41
.Lcu3_a:
	s_cmp_eq_u32 s7, 0
	s_cbranch_scc1 .LBB3_45
	s_add_i32 s25, s7, 1
	s_mov_b32 s7, 2
	s_cmp_eq_u32 s25, 2
	v_mov_b32_e32 v3, v6
	v_mov_b32_e32 v5, v47
	s_mov_b32 s19, s15
	s_cbranch_scc1 .LBB3_46
	s_cmp_eq_u32 s25, 3
	s_cselect_b64 vcc, -1, 0
	s_and_b64 s[26:27], vcc, exec
	v_cndmask_b32_e32 v5, 0, v48, vcc
	s_cselect_b32 s19, s6, 0x7fffffff
	s_mov_b32 s7, s25
	v_mov_b32_e32 v3, v7
	s_branch .LBB3_46

.LBB3_46:
	s_mov_b32 s25, 0
	s_branch .LBB3_47
.Lfl3_b:
	v_cmp_gt_i32_e32 vcc, 15, v18
	s_and_saveexec_b64 s[4:5], vcc
	s_cbranch_execz .LBB3_50
	v_max_i32_e32 v9, 1, v44
	v_cvt_f32_u32_e32 v9, v9
	v_rcp_iflag_f32_e32 v44, v9
	s_nop 0
	v_pk_mul_f32 v[10:11], v[44:45], s[2:3]
	s_nop 0
	v_mul_f32_e32 v14, 0x4b800000, v10
	v_pk_mul_f32 v[16:17], v[10:11], v[10:11] op_sel:[0,1] op_sel_hi:[1,0]
	s_nop 0
	v_pk_fma_f32 v[10:11], v[42:43], v[14:15], v[16:17] op_sel_hi:[1,0,0]
	v_fma_mixlo_f16 v9, v56, v14, v16
	v_pk_fma_f32 v[12:13], v[36:37], v[14:15], v[16:17] op_sel_hi:[1,0,0]
	v_pk_fma_f32 v[22:23], v[30:31], v[14:15], v[16:17] op_sel_hi:[1,0,0]
	v_cvt_pk_f16_f32 v11, v10, v11
	v_cvt_pk_f16_f32 v12, v12, v13
	v_pack_b32_f16 v10, v9, v11
	v_cvt_pk_f16_f32 v9, v22, v23
	v_alignbit_b32 v11, v12, v11, 16
	v_alignbit_b32 v12, v9, v12, 16
	v_lshrrev_b32_e32 v13, 16, v9
	v_add_u32_e32 v9, v18, v75
	v_fma_mixhi_f16 v13, v49, v14, v16
	v_xor_b32_e32 v14, v9, v0
	v_lshlrev_b32_e32 v14, 4, v14
	v_and_b32_e32 v14, 0xf0, v14
	v_lshl_or_b32 v9, v9, 8, v14
	ds_write_b128 v9, v[10:13]
